# nt cache policy on the read-once loads of the prologue x pass and the combine phases (x, y0, y1)
# speedup vs baseline: 1.0091x; 1.0081x over previous
.LBB0_148:
	v_readlane_b32 s1, v252, 21
	s_lshl_b32 s0, s55, 3
	s_ashr_i32 s1, s1, 6
	s_add_i32 s6, s1, s0
	s_cmpk_gt_i32 s6, 0x1fff
	v_mbcnt_lo_u32_b32 v72, -1, 0
	s_cbranch_scc1 .LBB0_161
	v_readlane_b32 s0, v252, 0
	s_lshl_b32 s10, s0, 3
	s_add_u32 s11, s70, 0x600000
	s_addc_u32 s14, s71, 0
	s_ashr_i32 s7, s6, 31
	s_lshl_b64 s[0:1], s[6:7], 13
	v_readlane_b32 s16, v252, 3
	s_waitcnt vmcnt(9)
	v_and_b32_e32 v34, 63, v132
	v_readlane_b32 s17, v252, 4
	s_add_u32 s0, s16, s0
	s_addc_u32 s1, s17, s1
	v_lshlrev_b32_e32 v64, 4, v34
	v_mov_b32_e32 v65, 0
	v_lshl_add_u64 v[16:17], s[0:1], 0, v[64:65]
	global_load_dwordx4 v[0:3], v64, s[0:1] nt
	global_load_dwordx4 v[4:7], v64, s[0:1] offset:1024 nt
	global_load_dwordx4 v[8:11], v64, s[0:1] offset:2048 nt
	global_load_dwordx4 v[12:15], v64, s[0:1] offset:3072 nt
	s_movk_i32 s0, 0x1000
	v_add_co_u32_e32 v32, vcc, s0, v16
	s_mov_b64 s[0:1], 0x21800000
	s_nop 0
	v_addc_co_u32_e32 v33, vcc, 0, v17, vcc
	global_load_dwordx4 v[16:19], v[32:33], off nt
	global_load_dwordx4 v[20:23], v[32:33], off offset:1024 nt
	global_load_dwordx4 v[24:27], v[32:33], off offset:2048 nt
	global_load_dwordx4 v[28:31], v[32:33], off offset:3072 nt
	v_mbcnt_hi_u32_b32 v32, -1, v72
	v_and_b32_e32 v33, 64, v32
	v_add_u32_e32 v33, 64, v33
	v_xor_b32_e32 v35, 1, v32
	v_cmp_lt_i32_e32 vcc, v35, v33
	v_lshl_add_u64 v[70:71], s[16:17], 0, v[64:65]
	v_mov_b32_e32 v64, 0x358637bd
	v_cndmask_b32_e32 v35, v32, v35, vcc
	v_lshlrev_b32_e32 v73, 2, v35
	v_xor_b32_e32 v35, 2, v32
	v_cmp_lt_i32_e32 vcc, v35, v33
	s_mov_b32 s15, 0xf800000
	v_mov_b32_e32 v79, 0x260
	v_cndmask_b32_e32 v35, v32, v35, vcc
	v_lshlrev_b32_e32 v74, 2, v35
	v_xor_b32_e32 v35, 4, v32
	v_cmp_lt_i32_e32 vcc, v35, v33
	s_mov_b32 s16, 0x40c0c00
	v_readlane_b32 s18, v252, 5
	v_cndmask_b32_e32 v35, v32, v35, vcc
	v_lshlrev_b32_e32 v75, 2, v35
	v_xor_b32_e32 v35, 8, v32
	v_cmp_lt_i32_e32 vcc, v35, v33
	v_readlane_b32 s19, v252, 6
	v_readlane_b32 s20, v252, 7
	v_cndmask_b32_e32 v35, v32, v35, vcc
	v_lshlrev_b32_e32 v76, 2, v35
	v_xor_b32_e32 v35, 16, v32
	v_cmp_lt_i32_e32 vcc, v35, v33
	v_readlane_b32 s21, v252, 8
	v_readlane_b32 s22, v252, 9
	v_cndmask_b32_e32 v35, v32, v35, vcc
	v_lshlrev_b32_e32 v77, 2, v35
	v_xor_b32_e32 v35, 32, v32
	v_cmp_lt_i32_e32 vcc, v35, v33
	v_mov_b32_e32 v33, v65
	v_readlane_b32 s23, v252, 10
	v_cndmask_b32_e32 v32, v32, v35, vcc
	v_lshlrev_b32_e32 v78, 2, v32
	v_lshlrev_b32_e32 v32, 3, v34
	v_lshl_add_u64 v[32:33], s[70:71], 0, v[32:33]
	v_lshl_add_u64 v[66:67], v[32:33], 0, s[0:1]
	v_lshlrev_b32_e32 v32, 2, v34
	v_mov_b32_e32 v33, v65
	v_lshl_add_u64 v[32:33], s[70:71], 0, v[32:33]
	s_mov_b64 s[0:1], 0x25800000
	v_lshl_add_u64 v[68:69], v[32:33], 0, s[0:1]
	v_cmp_eq_u32_e64 s[0:1], 0, v34
	v_readlane_b32 s24, v252, 11
	v_readlane_b32 s25, v252, 12
	v_readlane_b32 s26, v252, 13
	v_readlane_b32 s27, v252, 14
	v_readlane_b32 s28, v252, 15
	v_readlane_b32 s29, v252, 16
	v_readlane_b32 s30, v252, 17
	v_readlane_b32 s31, v252, 18
	s_branch .LBB0_152

.LBB0_152:
	s_add_i32 s2, s6, s10
	s_cmpk_lt_i32 s2, 0x2000
	s_cselect_b64 s[8:9], -1, 0
	s_cmpk_gt_i32 s2, 0x1fff
	s_cbranch_scc1 .LBB0_154
	s_ashr_i32 s3, s2, 31
	s_lshl_b64 s[4:5], s[2:3], 13
	s_waitcnt vmcnt(13)
	v_lshl_add_u64 v[48:49], v[70:71], 0, s[4:5]
	global_load_dwordx4 v[44:47], v[48:49], off nt
	global_load_dwordx4 v[40:43], v[48:49], off offset:1024 nt
	global_load_dwordx4 v[36:39], v[48:49], off offset:2048 nt
	global_load_dwordx4 v[32:35], v[48:49], off offset:3072 nt
	v_add_co_u32_e32 v48, vcc, 0x1000, v48
	s_nop 1
	v_addc_co_u32_e32 v49, vcc, 0, v49, vcc
	global_load_dwordx4 v[60:63], v[48:49], off nt
	global_load_dwordx4 v[56:59], v[48:49], off offset:1024 nt
	global_load_dwordx4 v[52:55], v[48:49], off offset:2048 nt
	s_nop 0
	global_load_dwordx4 v[48:51], v[48:49], off offset:3072 nt

.LBB0_157:
	s_add_i32 s6, s2, s10
	s_cmpk_lt_i32 s6, 0x2000
	s_cselect_b64 s[8:9], -1, 0
	s_cmpk_gt_i32 s6, 0x1fff
	s_cbranch_scc1 .LBB0_159
	s_ashr_i32 s7, s6, 31
	s_lshl_b64 s[4:5], s[6:7], 13
	v_lshl_add_u64 v[16:17], v[70:71], 0, s[4:5]
	v_add_co_u32_e32 v28, vcc, 0x1000, v16
	global_load_dwordx4 v[0:3], v[16:17], off nt
	global_load_dwordx4 v[4:7], v[16:17], off offset:1024 nt
	global_load_dwordx4 v[8:11], v[16:17], off offset:2048 nt
	global_load_dwordx4 v[12:15], v[16:17], off offset:3072 nt
	v_addc_co_u32_e32 v29, vcc, 0, v17, vcc
	global_load_dwordx4 v[16:19], v[28:29], off nt
	global_load_dwordx4 v[20:23], v[28:29], off offset:1024 nt
	global_load_dwordx4 v[24:27], v[28:29], off offset:2048 nt
	s_nop 0
	global_load_dwordx4 v[28:31], v[28:29], off offset:3072 nt

.LBB0_1859:
	s_or_b64 exec, exec, s[0:1]
	s_mov_b32 s1, s60
	s_waitcnt lgkmcnt(0)
	s_barrier
	s_lshl_b32 s0, s55, 3
	v_mbcnt_lo_u32_b32 v0, -1, s1
	v_mbcnt_hi_u32_b32 v0, -1, v0
	v_readlane_b32 s1, v252, 23
	s_nop 1
	v_add_u32_e32 v0, s1, v0
	s_nop 0
	v_readfirstlane_b32 s1, v0
	s_ashr_i32 s1, s1, 6
	s_add_i32 s8, s1, s0
	s_cmpk_gt_i32 s8, 0x1fff
	s_cbranch_scc1 .LBB0_1880
	v_readlane_b32 s10, v253, 9
	v_readlane_b32 s36, v252, 24
	s_lshl_b32 s7, s10, 3
	v_readlane_b32 s50, v252, 38
	v_readlane_b32 s51, v252, 39
	s_add_u32 s0, s50, 0x46800000
	s_addc_u32 s1, s51, 0
	v_and_b32_e32 v0, 63, v0
	s_ashr_i32 s9, s8, 31
	s_lshl_b64 s[2:3], s[8:9], 12
	v_lshlrev_b32_e32 v32, 3, v0
	v_or_b32_e32 v26, s2, v32
	v_mov_b32_e32 v27, s3
	v_or_b32_e32 v10, 0x200, v26
	v_mov_b32_e32 v11, s3
	v_or_b32_e32 v18, 0x400, v26
	v_mov_b32_e32 v19, s3
	v_lshl_add_u64 v[2:3], s[4:5], 0, v[26:27]
	v_lshl_add_u64 v[4:5], s[22:23], 0, v[26:27]
	v_lshl_add_u64 v[6:7], s[0:1], 0, v[26:27]
	v_lshl_add_u64 v[8:9], s[4:5], 0, v[10:11]
	v_lshl_add_u64 v[12:13], s[22:23], 0, v[10:11]
	v_lshl_add_u64 v[14:15], s[0:1], 0, v[10:11]
	v_lshl_add_u64 v[16:17], s[4:5], 0, v[18:19]
	v_lshl_add_u64 v[20:21], s[22:23], 0, v[18:19]
	global_load_dwordx2 v[2:3], v[2:3], off nt
	s_nop 0
	global_load_dwordx2 v[4:5], v[4:5], off nt
	s_nop 0
	global_load_dwordx2 v[6:7], v[6:7], off nt
	s_nop 0
	global_load_dwordx2 v[8:9], v[8:9], off nt
	s_nop 0
	global_load_dwordx2 v[10:11], v[12:13], off nt
	s_nop 0
	global_load_dwordx2 v[12:13], v[14:15], off nt
	s_nop 0
	global_load_dwordx2 v[14:15], v[16:17], off nt
	s_nop 0
	global_load_dwordx2 v[16:17], v[20:21], off nt
	v_or_b32_e32 v20, 0x600, v26
	v_mov_b32_e32 v21, s3
	v_lshl_add_u64 v[18:19], s[0:1], 0, v[18:19]
	v_lshl_add_u64 v[22:23], s[4:5], 0, v[20:21]
	v_lshl_add_u64 v[24:25], s[22:23], 0, v[20:21]
	v_lshl_add_u64 v[28:29], s[0:1], 0, v[20:21]
	global_load_dwordx2 v[18:19], v[18:19], off nt
	s_nop 0
	global_load_dwordx2 v[20:21], v[22:23], off nt
	s_nop 0
	global_load_dwordx2 v[22:23], v[24:25], off nt
	s_nop 0
	global_load_dwordx2 v[24:25], v[28:29], off nt
	v_or_b32_e32 v28, 0x800, v26
	v_mov_b32_e32 v29, s3
	v_or_b32_e32 v38, 0xa00, v26
	v_mov_b32_e32 v39, s3
	v_lshl_add_u64 v[30:31], s[4:5], 0, v[28:29]
	v_lshl_add_u64 v[34:35], s[22:23], 0, v[28:29]
	v_lshl_add_u64 v[36:37], s[0:1], 0, v[28:29]
	v_lshl_add_u64 v[40:41], s[4:5], 0, v[38:39]
	global_load_dwordx2 v[28:29], v[30:31], off nt
	s_nop 0
	global_load_dwordx2 v[30:31], v[34:35], off nt
	s_nop 0
	global_load_dwordx2 v[34:35], v[36:37], off nt
	s_nop 0
	global_load_dwordx2 v[36:37], v[40:41], off nt
	v_lshl_add_u64 v[40:41], s[22:23], 0, v[38:39]
	v_lshl_add_u64 v[38:39], s[0:1], 0, v[38:39]
	v_or_b32_e32 v42, 0xc00, v26
	v_mov_b32_e32 v43, s3
	v_lshl_add_u64 v[44:45], s[4:5], 0, v[42:43]
	v_lshl_add_u64 v[46:47], s[22:23], 0, v[42:43]
	global_load_dwordx2 v[54:55], v[40:41], off nt
	global_load_dwordx2 v[56:57], v[38:39], off nt
	global_load_dwordx2 v[60:61], v[44:45], off nt
	global_load_dwordx2 v[62:63], v[46:47], off nt
	v_lshl_add_u64 v[38:39], s[0:1], 0, v[42:43]
	v_or_b32_e32 v26, 0xe00, v26
	v_lshl_add_u64 v[40:41], s[4:5], 0, v[26:27]
	v_lshl_add_u64 v[42:43], s[22:23], 0, v[26:27]
	v_lshl_add_u64 v[26:27], s[0:1], 0, v[26:27]
	global_load_dwordx2 v[64:65], v[38:39], off nt
	global_load_dwordx2 v[66:67], v[40:41], off nt
	global_load_dwordx2 v[68:69], v[42:43], off nt
	global_load_dwordx2 v[70:71], v[26:27], off nt
	v_and_b32_e32 v1, 64, v188
	v_add_u32_e32 v26, 64, v1
	v_xor_b32_e32 v1, 1, v188
	v_cmp_lt_i32_e32 vcc, v1, v26
	v_xor_b32_e32 v27, 2, v188
	v_readlane_b32 s2, v252, 21
	v_cndmask_b32_e32 v1, v188, v1, vcc
	v_cmp_lt_i32_e32 vcc, v27, v26
	v_lshlrev_b32_e32 v172, 2, v0
	v_readlane_b32 s3, v252, 22
	v_cndmask_b32_e32 v27, v188, v27, vcc
	v_lshlrev_b32_e32 v41, 2, v27
	v_xor_b32_e32 v27, 4, v188
	v_cmp_lt_i32_e32 vcc, v27, v26
	v_readlane_b32 s46, v252, 34
	v_readlane_b32 s47, v252, 35
	v_cndmask_b32_e32 v27, v188, v27, vcc
	v_lshlrev_b32_e32 v45, 2, v27
	v_xor_b32_e32 v27, 8, v188
	v_cmp_lt_i32_e32 vcc, v27, v26
	v_or_b32_e32 v40, 0x100, v0
	v_or_b32_e32 v44, 0x140, v0
	v_cndmask_b32_e32 v27, v188, v27, vcc
	v_lshlrev_b32_e32 v49, 2, v27
	v_xor_b32_e32 v27, 16, v188
	v_cmp_lt_i32_e32 vcc, v27, v26
	v_or_b32_e32 v48, 0x180, v0
	v_or_b32_e32 v52, 0x1c0, v0
	v_cndmask_b32_e32 v27, v188, v27, vcc
	v_lshlrev_b32_e32 v53, 2, v27
	v_xor_b32_e32 v27, 32, v188
	v_cmp_lt_i32_e32 vcc, v27, v26
	v_mov_b32_e32 v33, v173
	v_lshlrev_b32_e32 v1, 2, v1
	v_cndmask_b32_e32 v26, v188, v27, vcc
	v_lshlrev_b32_e32 v153, 2, v26
	v_lshl_add_u64 v[26:27], s[2:3], 0, v[172:173]
	v_lshlrev_b32_e32 v172, 4, v0
	v_lshl_add_u64 v[38:39], s[46:47], 0, v[172:173]
	v_lshlrev_b32_e32 v172, 4, v40
	v_lshl_add_u64 v[42:43], s[46:47], 0, v[172:173]
	v_lshlrev_b32_e32 v172, 4, v44
	v_lshl_add_u64 v[46:47], s[46:47], 0, v[172:173]
	v_lshlrev_b32_e32 v172, 4, v48
	v_lshl_add_u64 v[50:51], s[46:47], 0, v[172:173]
	v_lshlrev_b32_e32 v172, 4, v52
	v_cmp_eq_u32_e64 s[34:35], 0, v0
	v_lshl_add_u64 v[32:33], s[4:5], 0, v[32:33]
	v_lshl_add_u64 v[58:59], s[46:47], 0, v[172:173]
	s_lshl_b32 s14, s10, 4
	v_readlane_b32 s37, v252, 25
	v_readlane_b32 s38, v252, 26
	v_readlane_b32 s39, v252, 27
	v_readlane_b32 s40, v252, 28
	v_readlane_b32 s41, v252, 29
	v_readlane_b32 s42, v252, 30
	v_readlane_b32 s43, v252, 31
	v_readlane_b32 s44, v252, 32
	v_readlane_b32 s45, v252, 33
	v_readlane_b32 s48, v252, 36
	v_readlane_b32 s49, v252, 37
	s_branch .LBB0_1863

.LBB0_1863:
	s_add_i32 s2, s8, s7
	s_cmpk_lt_i32 s2, 0x2000
	s_cselect_b64 s[10:11], -1, 0
	s_cmpk_gt_i32 s2, 0x1fff
	s_cbranch_scc1 .LBB0_1865
	s_ashr_i32 s3, s2, 31
	s_lshl_b64 s[12:13], s[2:3], 12
	v_lshl_or_b32 v110, v0, 3, s12
	v_mov_b32_e32 v111, s13
	v_or_b32_e32 v82, 0x200, v110
	v_mov_b32_e32 v83, s13
	v_lshl_add_u64 v[72:73], s[4:5], 0, v[110:111]
	v_lshl_add_u64 v[74:75], s[22:23], 0, v[110:111]
	v_lshl_add_u64 v[78:79], s[0:1], 0, v[110:111]
	v_lshl_add_u64 v[84:85], s[4:5], 0, v[82:83]
	v_or_b32_e32 v86, 0x400, v110
	v_mov_b32_e32 v87, s13
	global_load_dwordx2 v[72:73], v[72:73], off nt
	s_nop 0
	global_load_dwordx2 v[76:77], v[74:75], off nt
	global_load_dwordx2 v[80:81], v[78:79], off nt
	s_nop 0
	global_load_dwordx2 v[74:75], v[84:85], off nt
	v_lshl_add_u64 v[78:79], s[22:23], 0, v[82:83]
	v_lshl_add_u64 v[84:85], s[0:1], 0, v[82:83]
	v_lshl_add_u64 v[90:91], s[4:5], 0, v[86:87]
	v_lshl_add_u64 v[92:93], s[22:23], 0, v[86:87]
	global_load_dwordx2 v[82:83], v[78:79], off nt
	global_load_dwordx2 v[88:89], v[84:85], off nt
	s_nop 0
	global_load_dwordx2 v[78:79], v[90:91], off nt
	global_load_dwordx2 v[84:85], v[92:93], off nt
	v_or_b32_e32 v90, 0x600, v110
	v_mov_b32_e32 v91, s13
	v_lshl_add_u64 v[86:87], s[0:1], 0, v[86:87]
	v_lshl_add_u64 v[92:93], s[4:5], 0, v[90:91]
	v_lshl_add_u64 v[98:99], s[0:1], 0, v[90:91]
	v_lshl_add_u64 v[96:97], s[22:23], 0, v[90:91]
	global_load_dwordx2 v[94:95], v[86:87], off nt
	s_nop 0
	global_load_dwordx2 v[86:87], v[92:93], off nt
	global_load_dwordx2 v[90:91], v[96:97], off nt
	s_nop 0
	global_load_dwordx2 v[98:99], v[98:99], off nt
	v_or_b32_e32 v92, 0x800, v110
	v_mov_b32_e32 v93, s13
	v_or_b32_e32 v106, 0xa00, v110
	v_mov_b32_e32 v107, s13
	v_lshl_add_u64 v[96:97], s[4:5], 0, v[92:93]
	v_lshl_add_u64 v[100:101], s[22:23], 0, v[92:93]
	v_lshl_add_u64 v[102:103], s[0:1], 0, v[92:93]
	v_lshl_add_u64 v[108:109], s[4:5], 0, v[106:107]
	v_or_b32_e32 v114, 0xc00, v110
	v_mov_b32_e32 v115, s13
	global_load_dwordx2 v[92:93], v[96:97], off nt
	s_nop 0
	global_load_dwordx2 v[100:101], v[100:101], off nt
	s_nop 0
	global_load_dwordx2 v[104:105], v[102:103], off nt
	global_load_dwordx2 v[96:97], v[108:109], off nt
	v_lshl_add_u64 v[102:103], s[22:23], 0, v[106:107]
	v_lshl_add_u64 v[108:109], s[0:1], 0, v[106:107]
	v_lshl_add_u64 v[118:119], s[22:23], 0, v[114:115]
	v_or_b32_e32 v110, 0xe00, v110
	v_lshl_add_u64 v[116:117], s[4:5], 0, v[114:115]
	global_load_dwordx2 v[106:107], v[102:103], off nt
	global_load_dwordx2 v[112:113], v[108:109], off nt
	s_nop 0
	global_load_dwordx2 v[102:103], v[116:117], off nt
	global_load_dwordx2 v[108:109], v[118:119], off nt
	v_lshl_add_u64 v[114:115], s[0:1], 0, v[114:115]
	v_lshl_add_u64 v[118:119], s[4:5], 0, v[110:111]
	v_lshl_add_u64 v[120:121], s[22:23], 0, v[110:111]
	v_lshl_add_u64 v[122:123], s[0:1], 0, v[110:111]
	global_load_dwordx2 v[116:117], v[114:115], off nt
	global_load_dwordx2 v[110:111], v[118:119], off nt
	s_nop 0
	global_load_dwordx2 v[114:115], v[120:121], off nt
	global_load_dwordx2 v[118:119], v[122:123], off nt

.LBB0_1871:
	s_mov_b64 s[12:13], -1
	s_andn2_b64 vcc, exec, s[10:11]
	v_readfirstlane_b32 s3, v0
	s_cbranch_vccnz .LBB0_1862
	s_add_i32 s8, s14, s8
	s_cmpk_gt_i32 s8, 0x1fff
	s_cbranch_scc1 .LBB0_1874
	s_ashr_i32 s9, s8, 31
	s_lshl_b64 s[8:9], s[8:9], 12
	v_lshl_or_b32 v64, v0, 3, s8
	v_mov_b32_e32 v65, s9
	v_or_b32_e32 v10, 0x200, v64
	v_mov_b32_e32 v11, s9
	v_or_b32_e32 v18, 0x400, v64
	v_mov_b32_e32 v19, s9
	v_lshl_add_u64 v[2:3], s[4:5], 0, v[64:65]
	v_lshl_add_u64 v[4:5], s[22:23], 0, v[64:65]
	v_lshl_add_u64 v[6:7], s[0:1], 0, v[64:65]
	v_lshl_add_u64 v[8:9], s[4:5], 0, v[10:11]
	v_lshl_add_u64 v[12:13], s[22:23], 0, v[10:11]
	v_lshl_add_u64 v[14:15], s[0:1], 0, v[10:11]
	v_lshl_add_u64 v[16:17], s[4:5], 0, v[18:19]
	v_lshl_add_u64 v[20:21], s[22:23], 0, v[18:19]
	global_load_dwordx2 v[2:3], v[2:3], off nt
	s_nop 0
	global_load_dwordx2 v[4:5], v[4:5], off nt
	s_nop 0
	global_load_dwordx2 v[6:7], v[6:7], off nt
	s_nop 0
	global_load_dwordx2 v[8:9], v[8:9], off nt
	s_nop 0
	global_load_dwordx2 v[10:11], v[12:13], off nt
	s_nop 0
	global_load_dwordx2 v[12:13], v[14:15], off nt
	s_nop 0
	global_load_dwordx2 v[14:15], v[16:17], off nt
	s_nop 0
	global_load_dwordx2 v[16:17], v[20:21], off nt
	v_or_b32_e32 v20, 0x600, v64
	v_mov_b32_e32 v21, s9
	v_lshl_add_u64 v[18:19], s[0:1], 0, v[18:19]
	v_lshl_add_u64 v[22:23], s[4:5], 0, v[20:21]
	v_lshl_add_u64 v[24:25], s[22:23], 0, v[20:21]
	v_lshl_add_u64 v[28:29], s[0:1], 0, v[20:21]
	global_load_dwordx2 v[18:19], v[18:19], off nt
	s_nop 0
	global_load_dwordx2 v[20:21], v[22:23], off nt
	s_nop 0
	global_load_dwordx2 v[22:23], v[24:25], off nt
	s_nop 0
	global_load_dwordx2 v[24:25], v[28:29], off nt
	v_or_b32_e32 v28, 0x800, v64
	v_mov_b32_e32 v29, s9
	v_or_b32_e32 v54, 0xa00, v64
	v_mov_b32_e32 v55, s9
	v_lshl_add_u64 v[30:31], s[4:5], 0, v[28:29]
	v_lshl_add_u64 v[34:35], s[22:23], 0, v[28:29]
	v_lshl_add_u64 v[36:37], s[0:1], 0, v[28:29]
	v_lshl_add_u64 v[56:57], s[4:5], 0, v[54:55]
	v_or_b32_e32 v66, 0xc00, v64
	v_mov_b32_e32 v67, s9
	global_load_dwordx2 v[28:29], v[30:31], off nt
	s_nop 0
	global_load_dwordx2 v[30:31], v[34:35], off nt
	s_nop 0
	global_load_dwordx2 v[34:35], v[36:37], off nt
	s_nop 0
	global_load_dwordx2 v[36:37], v[56:57], off nt
	v_lshl_add_u64 v[56:57], s[22:23], 0, v[54:55]
	v_lshl_add_u64 v[60:61], s[0:1], 0, v[54:55]
	v_lshl_add_u64 v[62:63], s[4:5], 0, v[66:67]
	v_lshl_add_u64 v[68:69], s[22:23], 0, v[66:67]
	v_or_b32_e32 v64, 0xe00, v64
	global_load_dwordx2 v[54:55], v[56:57], off nt
	s_nop 0
	global_load_dwordx2 v[56:57], v[60:61], off nt
	s_nop 0
	global_load_dwordx2 v[60:61], v[62:63], off nt
	s_nop 0
	global_load_dwordx2 v[62:63], v[68:69], off nt
	v_lshl_add_u64 v[66:67], s[0:1], 0, v[66:67]
	v_lshl_add_u64 v[68:69], s[4:5], 0, v[64:65]
	v_lshl_add_u64 v[70:71], s[22:23], 0, v[64:65]
	v_lshl_add_u64 v[120:121], s[0:1], 0, v[64:65]
	global_load_dwordx2 v[64:65], v[66:67], off nt
	s_nop 0
	global_load_dwordx2 v[66:67], v[68:69], off nt
	s_nop 0
	global_load_dwordx2 v[68:69], v[70:71], off nt
	s_nop 0
	global_load_dwordx2 v[70:71], v[120:121], off nt
